# DSA attention: the first four transposed V reads of the PV stage issued ahead of the accumulator rescale so their LDS latency runs under the 16 pk_mul
# baseline (speedup 1.0000x reference)
.Lat_A_full:
	v_max3_f32 v92, v82, v83, v84
	v_max3_f32 v93, v85, v86, v87
	v_max3_f32 v92, v92, v88, v89
	v_max_f32_e32 v92, v92, v93
	v_mov_b32_e32 v93, v92
	s_nop 1
	v_permlane16_swap_b32_e32 v92, v93
	v_max_f32_e32 v92, v92, v93
	v_mov_b32_e32 v93, v92
	s_nop 1
	v_permlane32_swap_b32_e32 v92, v93
	v_max3_f32 v180, v181, v92, v93
	v_sub_f32_e32 v94, v181, v180
	v_sub_f32_e32 v82, v82, v180
	v_sub_f32_e32 v83, v83, v180
	v_sub_f32_e32 v84, v84, v180
	v_sub_f32_e32 v85, v85, v180
	v_sub_f32_e32 v86, v86, v180
	v_sub_f32_e32 v87, v87, v180
	v_sub_f32_e32 v88, v88, v180
	v_sub_f32_e32 v89, v89, v180
	v_exp_f32_e32 v94, v94
	v_exp_f32_e32 v82, v82
	v_exp_f32_e32 v83, v83
	v_exp_f32_e32 v84, v84
	v_exp_f32_e32 v85, v85
	v_exp_f32_e32 v86, v86
	v_exp_f32_e32 v87, v87
	v_exp_f32_e32 v88, v88
	v_exp_f32_e32 v89, v89
	v_add_f32_e32 v92, v82, v83
	v_add_f32_e32 v93, v84, v85
	v_add_f32_e32 v97, v86, v87
	v_add_f32_e32 v92, v92, v93
	v_add_f32_e32 v96, v88, v89
	v_add_f32_e32 v97, v97, v96
	v_add_f32_e32 v92, v92, v97
	v_mov_b32_e32 v93, v92
	v_mov_b32_e32 v181, v180
	v_cvt_pk_bf16_f32 v82, v82, v83
	v_cvt_pk_bf16_f32 v83, v84, v85
	v_permlane16_swap_b32_e32 v92, v93
	v_add_f32_e32 v92, v92, v93
	v_mov_b32_e32 v93, v92
	v_cvt_pk_bf16_f32 v84, v86, v87
	v_cvt_pk_bf16_f32 v85, v88, v89
	ds_read_b64_tr_b16 v[86:87], v231
	ds_read_b64_tr_b16 v[88:89], v231 offset:4096
	ds_read_b64_tr_b16 v[244:245], v232
	ds_read_b64_tr_b16 v[246:247], v232 offset:4096
	v_permlane32_swap_b32_e32 v92, v93
	v_add_f32_e32 v92, v92, v93
	v_fma_f32 v179, v179, v94, v92
	v_pk_mul_f32 v[2:3], v[2:3], v[94:95] op_sel_hi:[1,0]
	v_pk_mul_f32 v[4:5], v[4:5], v[94:95] op_sel_hi:[1,0]
	v_pk_mul_f32 v[6:7], v[6:7], v[94:95] op_sel_hi:[1,0]
	v_pk_mul_f32 v[8:9], v[8:9], v[94:95] op_sel_hi:[1,0]
	v_pk_mul_f32 v[10:11], v[10:11], v[94:95] op_sel_hi:[1,0]
	v_pk_mul_f32 v[12:13], v[12:13], v[94:95] op_sel_hi:[1,0]
	v_pk_mul_f32 v[14:15], v[14:15], v[94:95] op_sel_hi:[1,0]
	v_pk_mul_f32 v[16:17], v[16:17], v[94:95] op_sel_hi:[1,0]
	v_pk_mul_f32 v[18:19], v[18:19], v[94:95] op_sel_hi:[1,0]
	v_pk_mul_f32 v[20:21], v[20:21], v[94:95] op_sel_hi:[1,0]
	v_pk_mul_f32 v[22:23], v[22:23], v[94:95] op_sel_hi:[1,0]
	v_pk_mul_f32 v[24:25], v[24:25], v[94:95] op_sel_hi:[1,0]
	v_pk_mul_f32 v[26:27], v[26:27], v[94:95] op_sel_hi:[1,0]
	v_pk_mul_f32 v[28:29], v[28:29], v[94:95] op_sel_hi:[1,0]
	v_pk_mul_f32 v[30:31], v[30:31], v[94:95] op_sel_hi:[1,0]
	v_pk_mul_f32 v[32:33], v[32:33], v[94:95] op_sel_hi:[1,0]
	s_waitcnt lgkmcnt(2)
	v_mfma_f32_16x16x32_bf16 v[2:5], v[86:89], v[82:85], v[2:5]
	ds_read_b64_tr_b16 v[86:87], v233
	ds_read_b64_tr_b16 v[88:89], v233 offset:4096
	s_waitcnt lgkmcnt(2)
	v_mfma_f32_16x16x32_bf16 v[6:9], v[244:247], v[82:85], v[6:9]
	ds_read_b64_tr_b16 v[244:245], v234
	ds_read_b64_tr_b16 v[246:247], v234 offset:4096
	s_waitcnt lgkmcnt(2)
	v_mfma_f32_16x16x32_bf16 v[10:13], v[86:89], v[82:85], v[10:13]
	ds_read_b64_tr_b16 v[86:87], v235
	ds_read_b64_tr_b16 v[88:89], v235 offset:4096
	s_waitcnt lgkmcnt(2)
	v_mfma_f32_16x16x32_bf16 v[14:17], v[244:247], v[82:85], v[14:17]
	ds_read_b64_tr_b16 v[244:245], v236
	ds_read_b64_tr_b16 v[246:247], v236 offset:4096
	s_waitcnt lgkmcnt(2)
	v_mfma_f32_16x16x32_bf16 v[18:21], v[86:89], v[82:85], v[18:21]
	ds_read_b64_tr_b16 v[86:87], v237
	ds_read_b64_tr_b16 v[88:89], v237 offset:4096
	s_waitcnt lgkmcnt(2)
	v_mfma_f32_16x16x32_bf16 v[22:25], v[244:247], v[82:85], v[22:25]
	ds_read_b64_tr_b16 v[244:245], v238
	ds_read_b64_tr_b16 v[246:247], v238 offset:4096
	s_waitcnt lgkmcnt(2)
	v_mfma_f32_16x16x32_bf16 v[30:33], v[86:89], v[82:85], v[30:33]
	s_waitcnt lgkmcnt(0)
	v_mfma_f32_16x16x32_bf16 v[26:29], v[244:247], v[82:85], v[26:29]
	s_add_u32 s11, s11, 1
	s_add_u32 s22, s22, 32
	v_add_u32_e32 v239, 0x80, v239
	s_cmp_lt_u32 s11, s10
	s_cbranch_scc0 .Lat_done

.Lat_B_full:
	v_max3_f32 v92, v82, v83, v84
	v_max3_f32 v93, v85, v86, v87
	v_max3_f32 v92, v92, v88, v89
	v_max_f32_e32 v92, v92, v93
	v_mov_b32_e32 v93, v92
	s_nop 1
	v_permlane16_swap_b32_e32 v92, v93
	v_max_f32_e32 v92, v92, v93
	v_mov_b32_e32 v93, v92
	s_nop 1
	v_permlane32_swap_b32_e32 v92, v93
	v_max3_f32 v180, v181, v92, v93
	v_sub_f32_e32 v94, v181, v180
	v_sub_f32_e32 v82, v82, v180
	v_sub_f32_e32 v83, v83, v180
	v_sub_f32_e32 v84, v84, v180
	v_sub_f32_e32 v85, v85, v180
	v_sub_f32_e32 v86, v86, v180
	v_sub_f32_e32 v87, v87, v180
	v_sub_f32_e32 v88, v88, v180
	v_sub_f32_e32 v89, v89, v180
	v_exp_f32_e32 v94, v94
	v_exp_f32_e32 v82, v82
	v_exp_f32_e32 v83, v83
	v_exp_f32_e32 v84, v84
	v_exp_f32_e32 v85, v85
	v_exp_f32_e32 v86, v86
	v_exp_f32_e32 v87, v87
	v_exp_f32_e32 v88, v88
	v_exp_f32_e32 v89, v89
	v_add_f32_e32 v92, v82, v83
	v_add_f32_e32 v93, v84, v85
	v_add_f32_e32 v97, v86, v87
	v_add_f32_e32 v92, v92, v93
	v_add_f32_e32 v96, v88, v89
	v_add_f32_e32 v97, v97, v96
	v_add_f32_e32 v92, v92, v97
	v_mov_b32_e32 v93, v92
	v_mov_b32_e32 v181, v180
	v_cvt_pk_bf16_f32 v82, v82, v83
	v_cvt_pk_bf16_f32 v83, v84, v85
	v_permlane16_swap_b32_e32 v92, v93
	v_add_f32_e32 v92, v92, v93
	v_mov_b32_e32 v93, v92
	v_cvt_pk_bf16_f32 v84, v86, v87
	v_cvt_pk_bf16_f32 v85, v88, v89
	ds_read_b64_tr_b16 v[86:87], v231
	ds_read_b64_tr_b16 v[88:89], v231 offset:4096
	ds_read_b64_tr_b16 v[244:245], v232
	ds_read_b64_tr_b16 v[246:247], v232 offset:4096
	v_permlane32_swap_b32_e32 v92, v93
	v_add_f32_e32 v92, v92, v93
	v_fma_f32 v179, v179, v94, v92
	v_pk_mul_f32 v[2:3], v[2:3], v[94:95] op_sel_hi:[1,0]
	v_pk_mul_f32 v[4:5], v[4:5], v[94:95] op_sel_hi:[1,0]
	v_pk_mul_f32 v[6:7], v[6:7], v[94:95] op_sel_hi:[1,0]
	v_pk_mul_f32 v[8:9], v[8:9], v[94:95] op_sel_hi:[1,0]
	v_pk_mul_f32 v[10:11], v[10:11], v[94:95] op_sel_hi:[1,0]
	v_pk_mul_f32 v[12:13], v[12:13], v[94:95] op_sel_hi:[1,0]
	v_pk_mul_f32 v[14:15], v[14:15], v[94:95] op_sel_hi:[1,0]
	v_pk_mul_f32 v[16:17], v[16:17], v[94:95] op_sel_hi:[1,0]
	v_pk_mul_f32 v[18:19], v[18:19], v[94:95] op_sel_hi:[1,0]
	v_pk_mul_f32 v[20:21], v[20:21], v[94:95] op_sel_hi:[1,0]
	v_pk_mul_f32 v[22:23], v[22:23], v[94:95] op_sel_hi:[1,0]
	v_pk_mul_f32 v[24:25], v[24:25], v[94:95] op_sel_hi:[1,0]
	v_pk_mul_f32 v[26:27], v[26:27], v[94:95] op_sel_hi:[1,0]
	v_pk_mul_f32 v[28:29], v[28:29], v[94:95] op_sel_hi:[1,0]
	v_pk_mul_f32 v[30:31], v[30:31], v[94:95] op_sel_hi:[1,0]
	v_pk_mul_f32 v[32:33], v[32:33], v[94:95] op_sel_hi:[1,0]
	s_waitcnt lgkmcnt(2)
	v_mfma_f32_16x16x32_bf16 v[2:5], v[86:89], v[82:85], v[2:5]
	ds_read_b64_tr_b16 v[86:87], v233
	ds_read_b64_tr_b16 v[88:89], v233 offset:4096
	s_waitcnt lgkmcnt(2)
	v_mfma_f32_16x16x32_bf16 v[6:9], v[244:247], v[82:85], v[6:9]
	ds_read_b64_tr_b16 v[244:245], v234
	ds_read_b64_tr_b16 v[246:247], v234 offset:4096
	s_waitcnt lgkmcnt(2)
	v_mfma_f32_16x16x32_bf16 v[10:13], v[86:89], v[82:85], v[10:13]
	ds_read_b64_tr_b16 v[86:87], v235
	ds_read_b64_tr_b16 v[88:89], v235 offset:4096
	s_waitcnt lgkmcnt(2)
	v_mfma_f32_16x16x32_bf16 v[14:17], v[244:247], v[82:85], v[14:17]
	ds_read_b64_tr_b16 v[244:245], v236
	ds_read_b64_tr_b16 v[246:247], v236 offset:4096
	s_waitcnt lgkmcnt(2)
	v_mfma_f32_16x16x32_bf16 v[18:21], v[86:89], v[82:85], v[18:21]
	ds_read_b64_tr_b16 v[86:87], v237
	ds_read_b64_tr_b16 v[88:89], v237 offset:4096
	s_waitcnt lgkmcnt(2)
	v_mfma_f32_16x16x32_bf16 v[22:25], v[244:247], v[82:85], v[22:25]
	ds_read_b64_tr_b16 v[244:245], v238
	ds_read_b64_tr_b16 v[246:247], v238 offset:4096
	s_waitcnt lgkmcnt(2)
	v_mfma_f32_16x16x32_bf16 v[30:33], v[86:89], v[82:85], v[30:33]
	s_waitcnt lgkmcnt(0)
	v_mfma_f32_16x16x32_bf16 v[26:29], v[244:247], v[82:85], v[26:29]
	s_add_u32 s11, s11, 1
	s_add_u32 s22, s22, 32
	v_add_u32_e32 v239, 0x80, v239
	s_cmp_lt_u32 s11, s10
	s_cbranch_scc1 .Lat_A
